# P1: non-temporal stores for the sigmoid branch-gate columns (written first, not read before P4)
# baseline (speedup 1.0000x reference)
.LBB0_173:
	s_lshl_b32 s1, s1, 11
	s_and_b32 s1, s1, 0x800
	s_add_i32 s1, s1, 0
	s_lshl_b32 s11, s0, 8
	s_add_i32 s1, s1, 0x25500
	s_add_i32 s11, s11, s57
	s_cmp_lt_i32 s10, 44
	s_cselect_b32 s0, 1, 2
	s_lshl_b32 s4, s20, 2
	s_add_i32 s4, s1, s4
	v_lshl_add_u32 v110, v160, 2, s4
	s_lshl_b32 s4, s57, 2
	s_add_i32 s1, s1, s4
	v_lshl_add_u32 v146, v167, 2, s1
	ds_read_b128 v[114:117], v110 offset:1024
	ds_read_b128 v[118:121], v110 offset:1040
	ds_read_b128 v[106:109], v110 offset:1536
	ds_read_b128 v[110:113], v110 offset:1552
	ds_read2_b32 v[188:189], v146 offset1:16
	ds_read2_b32 v[186:187], v146 offset0:32 offset1:48
	ds_read2_b32 v[184:185], v146 offset0:128 offset1:144
	ds_read2_b32 v[182:183], v146 offset0:160 offset1:176
	s_cmp_gt_i32 s10, 35
	s_cselect_b32 s4, s0, 0
	v_or_b32_e32 v146, s11, v167
	s_cmp_lt_i32 s4, 1
	s_mov_b64 s[0:1], -1
	s_cbranch_scc1 .LBB0_180
	v_lshl_or_b32 v190, s10, 8, v197
	s_cmp_lg_u32 s4, 1
	v_ashrrev_i32_e32 v191, 31, v190
	v_or_b32_e32 v203, 16, v146
	v_or_b32_e32 v202, 32, v146
	v_or_b32_e32 v201, 48, v146
	s_cbranch_scc0 .LBB0_176
	v_mov_b64_e32 v[192:193], s[88:89]
	v_mad_i64_i32 v[204:205], s[0:1], v146, s62, v[192:193]
	v_lshlrev_b64 v[194:195], 1, v[190:191]
	v_lshl_add_u64 v[208:209], v[204:205], 0, v[194:195]
	v_cvt_f32_i32_e32 v205, v143
	v_cvt_f32_i32_e32 v207, v145
	v_cvt_f32_i32_e32 v206, v144
	v_cvt_f32_i32_e32 v204, v142
	s_waitcnt lgkmcnt(0)
	v_mul_f32_e32 v210, 0xbfb8aa3b, v188
	v_pk_mul_f32 v[212:213], v[116:117], v[210:211] op_sel_hi:[1,0]
	v_pk_mul_f32 v[214:215], v[114:115], v[210:211] op_sel_hi:[1,0]
	v_pk_mul_f32 v[206:207], v[212:213], v[206:207]
	v_pk_mul_f32 v[204:205], v[214:215], v[204:205]
	v_cvt_f32_i32_e32 v213, v139
	v_cvt_f32_i32_e32 v215, v141
	v_cvt_f32_i32_e32 v214, v140
	v_cvt_f32_i32_e32 v212, v138
	v_pk_mul_f32 v[216:217], v[120:121], v[210:211] op_sel_hi:[1,0]
	v_pk_mul_f32 v[218:219], v[118:119], v[210:211] op_sel_hi:[1,0]
	v_pk_mul_f32 v[214:215], v[216:217], v[214:215]
	v_pk_mul_f32 v[212:213], v[218:219], v[212:213]
	v_exp_f32_e32 v204, v204
	v_exp_f32_e32 v205, v205
	v_exp_f32_e32 v206, v206
	v_exp_f32_e32 v207, v207
	v_exp_f32_e32 v212, v212
	v_exp_f32_e32 v214, v214
	v_exp_f32_e32 v215, v215
	v_exp_f32_e32 v213, v213
	v_pk_add_f32 v[206:207], v[206:207], 1.0 op_sel_hi:[1,0]
	v_pk_add_f32 v[204:205], v[204:205], 1.0 op_sel_hi:[1,0]
	v_pk_add_f32 v[214:215], v[214:215], 1.0 op_sel_hi:[1,0]
	v_pk_add_f32 v[212:213], v[212:213], 1.0 op_sel_hi:[1,0]
	v_rcp_f32_e32 v204, v204
	v_rcp_f32_e32 v205, v205
	v_rcp_f32_e32 v206, v206
	v_rcp_f32_e32 v207, v207
	v_rcp_f32_e32 v211, v212
	v_rcp_f32_e32 v212, v213
	v_rcp_f32_e32 v213, v214
	v_rcp_f32_e32 v214, v215
	v_cvt_pk_bf16_f32 v204, v204, v205
	v_cvt_pk_bf16_f32 v205, v206, v207
	v_cvt_pk_bf16_f32 v206, v211, v212
	v_cvt_pk_bf16_f32 v207, v213, v214
	global_store_dwordx4 v[208:209], v[204:207], off nt
	v_pk_mul_f32 v[212:213], v[108:109], v[210:211] op_sel_hi:[1,0]
	v_pk_mul_f32 v[214:215], v[106:107], v[210:211] op_sel_hi:[1,0]
	v_cvt_f32_i32_e32 v205, v135
	v_cvt_f32_i32_e32 v207, v137
	v_cvt_f32_i32_e32 v206, v136
	v_cvt_f32_i32_e32 v204, v134
	v_pk_mul_f32 v[216:217], v[112:113], v[210:211] op_sel_hi:[1,0]
	v_pk_mul_f32 v[210:211], v[110:111], v[210:211] op_sel_hi:[1,0]
	v_pk_mul_f32 v[206:207], v[212:213], v[206:207]
	v_pk_mul_f32 v[204:205], v[214:215], v[204:205]
	v_cvt_f32_i32_e32 v213, v131
	v_cvt_f32_i32_e32 v215, v133
	v_cvt_f32_i32_e32 v214, v132
	v_cvt_f32_i32_e32 v212, v130
	v_exp_f32_e32 v204, v204
	v_exp_f32_e32 v205, v205
	v_pk_mul_f32 v[214:215], v[216:217], v[214:215]
	v_pk_mul_f32 v[210:211], v[210:211], v[212:213]
	v_exp_f32_e32 v206, v206
	v_exp_f32_e32 v207, v207
	v_exp_f32_e32 v210, v210
	v_exp_f32_e32 v212, v214
	v_exp_f32_e32 v213, v215
	v_exp_f32_e32 v211, v211
	v_pk_add_f32 v[204:205], v[204:205], 1.0 op_sel_hi:[1,0]
	v_pk_add_f32 v[206:207], v[206:207], 1.0 op_sel_hi:[1,0]
	v_rcp_f32_e32 v204, v204
	v_rcp_f32_e32 v205, v205
	v_pk_add_f32 v[212:213], v[212:213], 1.0 op_sel_hi:[1,0]
	v_pk_add_f32 v[210:211], v[210:211], 1.0 op_sel_hi:[1,0]
	v_rcp_f32_e32 v206, v206
	v_rcp_f32_e32 v207, v207
	v_cvt_pk_bf16_f32 v204, v204, v205
	v_cvt_pk_bf16_f32 v205, v206, v207
	v_rcp_f32_e32 v210, v210
	v_rcp_f32_e32 v211, v211
	v_rcp_f32_e32 v212, v212
	v_rcp_f32_e32 v213, v213
	v_cvt_pk_bf16_f32 v206, v210, v211
	v_cvt_pk_bf16_f32 v207, v212, v213
	global_store_dwordx4 v[208:209], v[204:207], off offset:256 nt
	v_mul_f32_e32 v210, 0xbfb8aa3b, v189
	v_pk_mul_f32 v[212:213], v[116:117], v[210:211] op_sel_hi:[1,0]
	v_mad_i64_i32 v[204:205], s[0:1], v203, s62, v[192:193]
	v_lshl_add_u64 v[208:209], v[204:205], 0, v[194:195]
	v_cvt_f32_i32_e32 v205, v123
	v_cvt_f32_i32_e32 v207, v125
	v_cvt_f32_i32_e32 v206, v124
	v_cvt_f32_i32_e32 v204, v122
	v_pk_mul_f32 v[214:215], v[114:115], v[210:211] op_sel_hi:[1,0]
	v_pk_mul_f32 v[216:217], v[120:121], v[210:211] op_sel_hi:[1,0]
	v_pk_mul_f32 v[206:207], v[212:213], v[206:207]
	v_pk_mul_f32 v[204:205], v[214:215], v[204:205]
	v_cvt_f32_i32_e32 v213, v127
	v_cvt_f32_i32_e32 v215, v129
	v_cvt_f32_i32_e32 v214, v128
	v_cvt_f32_i32_e32 v212, v126
	v_pk_mul_f32 v[218:219], v[118:119], v[210:211] op_sel_hi:[1,0]
	v_exp_f32_e32 v204, v204
	v_pk_mul_f32 v[214:215], v[216:217], v[214:215]
	v_pk_mul_f32 v[212:213], v[218:219], v[212:213]
	v_exp_f32_e32 v205, v205
	v_exp_f32_e32 v206, v206
	v_exp_f32_e32 v207, v207
	v_exp_f32_e32 v212, v212
	v_exp_f32_e32 v214, v214
	v_exp_f32_e32 v215, v215
	v_exp_f32_e32 v213, v213
	v_pk_add_f32 v[206:207], v[206:207], 1.0 op_sel_hi:[1,0]
	v_pk_add_f32 v[204:205], v[204:205], 1.0 op_sel_hi:[1,0]
	v_pk_add_f32 v[214:215], v[214:215], 1.0 op_sel_hi:[1,0]
	v_pk_add_f32 v[212:213], v[212:213], 1.0 op_sel_hi:[1,0]
	v_rcp_f32_e32 v204, v204
	v_rcp_f32_e32 v205, v205
	v_rcp_f32_e32 v206, v206
	v_rcp_f32_e32 v207, v207
	v_rcp_f32_e32 v211, v212
	v_rcp_f32_e32 v212, v213
	v_rcp_f32_e32 v213, v214
	v_rcp_f32_e32 v214, v215
	v_cvt_pk_bf16_f32 v204, v204, v205
	v_cvt_pk_bf16_f32 v205, v206, v207
	v_cvt_pk_bf16_f32 v206, v211, v212
	v_cvt_pk_bf16_f32 v207, v213, v214
	global_store_dwordx4 v[208:209], v[204:207], off nt
	v_pk_mul_f32 v[212:213], v[108:109], v[210:211] op_sel_hi:[1,0]
	v_pk_mul_f32 v[214:215], v[106:107], v[210:211] op_sel_hi:[1,0]
	v_cvt_f32_i32_e32 v205, v99
	v_cvt_f32_i32_e32 v207, v101
	v_cvt_f32_i32_e32 v206, v100
	v_cvt_f32_i32_e32 v204, v98
	v_pk_mul_f32 v[216:217], v[112:113], v[210:211] op_sel_hi:[1,0]
	v_pk_mul_f32 v[210:211], v[110:111], v[210:211] op_sel_hi:[1,0]
	v_pk_mul_f32 v[206:207], v[212:213], v[206:207]
	v_pk_mul_f32 v[204:205], v[214:215], v[204:205]
	v_cvt_f32_i32_e32 v213, v103
	v_cvt_f32_i32_e32 v215, v105
	v_cvt_f32_i32_e32 v214, v104
	v_cvt_f32_i32_e32 v212, v102
	v_exp_f32_e32 v204, v204
	v_exp_f32_e32 v205, v205
	v_pk_mul_f32 v[214:215], v[216:217], v[214:215]
	v_pk_mul_f32 v[210:211], v[210:211], v[212:213]
	v_exp_f32_e32 v206, v206
	v_exp_f32_e32 v207, v207
	v_exp_f32_e32 v210, v210
	v_exp_f32_e32 v212, v214
	v_exp_f32_e32 v213, v215
	v_exp_f32_e32 v211, v211
	v_pk_add_f32 v[204:205], v[204:205], 1.0 op_sel_hi:[1,0]
	v_pk_add_f32 v[206:207], v[206:207], 1.0 op_sel_hi:[1,0]
	v_rcp_f32_e32 v204, v204
	v_rcp_f32_e32 v205, v205
	v_pk_add_f32 v[212:213], v[212:213], 1.0 op_sel_hi:[1,0]
	v_pk_add_f32 v[210:211], v[210:211], 1.0 op_sel_hi:[1,0]
	v_rcp_f32_e32 v206, v206
	v_rcp_f32_e32 v207, v207
	v_cvt_pk_bf16_f32 v204, v204, v205
	v_cvt_pk_bf16_f32 v205, v206, v207
	v_rcp_f32_e32 v210, v210
	v_rcp_f32_e32 v211, v211
	v_rcp_f32_e32 v212, v212
	v_rcp_f32_e32 v213, v213
	v_cvt_pk_bf16_f32 v206, v210, v211
	v_cvt_pk_bf16_f32 v207, v212, v213
	global_store_dwordx4 v[208:209], v[204:207], off offset:256 nt
	v_mul_f32_e32 v210, 0xbfb8aa3b, v186
	v_pk_mul_f32 v[212:213], v[116:117], v[210:211] op_sel_hi:[1,0]
	v_mad_i64_i32 v[204:205], s[0:1], v202, s62, v[192:193]
	v_lshl_add_u64 v[208:209], v[204:205], 0, v[194:195]
	v_cvt_f32_i32_e32 v205, v95
	v_cvt_f32_i32_e32 v207, v97
	v_cvt_f32_i32_e32 v206, v96
	v_cvt_f32_i32_e32 v204, v94
	v_pk_mul_f32 v[214:215], v[114:115], v[210:211] op_sel_hi:[1,0]
	v_pk_mul_f32 v[216:217], v[120:121], v[210:211] op_sel_hi:[1,0]
	v_pk_mul_f32 v[206:207], v[212:213], v[206:207]
	v_pk_mul_f32 v[204:205], v[214:215], v[204:205]
	v_cvt_f32_i32_e32 v213, v91
	v_cvt_f32_i32_e32 v215, v93
	v_cvt_f32_i32_e32 v214, v92
	v_cvt_f32_i32_e32 v212, v90
	v_pk_mul_f32 v[218:219], v[118:119], v[210:211] op_sel_hi:[1,0]
	v_exp_f32_e32 v204, v204
	v_pk_mul_f32 v[214:215], v[216:217], v[214:215]
	v_pk_mul_f32 v[212:213], v[218:219], v[212:213]
	v_exp_f32_e32 v205, v205
	v_exp_f32_e32 v206, v206
	v_exp_f32_e32 v207, v207
	v_exp_f32_e32 v212, v212
	v_exp_f32_e32 v214, v214
	v_exp_f32_e32 v215, v215
	v_exp_f32_e32 v213, v213
	v_pk_add_f32 v[206:207], v[206:207], 1.0 op_sel_hi:[1,0]
	v_pk_add_f32 v[204:205], v[204:205], 1.0 op_sel_hi:[1,0]
	v_pk_add_f32 v[214:215], v[214:215], 1.0 op_sel_hi:[1,0]
	v_pk_add_f32 v[212:213], v[212:213], 1.0 op_sel_hi:[1,0]
	v_rcp_f32_e32 v204, v204
	v_rcp_f32_e32 v205, v205
	v_rcp_f32_e32 v206, v206
	v_rcp_f32_e32 v207, v207
	v_rcp_f32_e32 v211, v212
	v_rcp_f32_e32 v212, v213
	v_rcp_f32_e32 v213, v214
	v_rcp_f32_e32 v214, v215
	v_cvt_pk_bf16_f32 v204, v204, v205
	v_cvt_pk_bf16_f32 v205, v206, v207
	v_cvt_pk_bf16_f32 v206, v211, v212
	v_cvt_pk_bf16_f32 v207, v213, v214
	global_store_dwordx4 v[208:209], v[204:207], off nt
	v_pk_mul_f32 v[212:213], v[108:109], v[210:211] op_sel_hi:[1,0]
	v_pk_mul_f32 v[214:215], v[106:107], v[210:211] op_sel_hi:[1,0]
	v_cvt_f32_i32_e32 v205, v87
	v_cvt_f32_i32_e32 v207, v89
	v_cvt_f32_i32_e32 v206, v88
	v_cvt_f32_i32_e32 v204, v86
	v_pk_mul_f32 v[216:217], v[112:113], v[210:211] op_sel_hi:[1,0]
	v_pk_mul_f32 v[210:211], v[110:111], v[210:211] op_sel_hi:[1,0]
	v_pk_mul_f32 v[206:207], v[212:213], v[206:207]
	v_pk_mul_f32 v[204:205], v[214:215], v[204:205]
	v_cvt_f32_i32_e32 v213, v79
	v_cvt_f32_i32_e32 v215, v81
	v_cvt_f32_i32_e32 v214, v80
	v_cvt_f32_i32_e32 v212, v78
	v_exp_f32_e32 v204, v204
	v_exp_f32_e32 v205, v205
	v_pk_mul_f32 v[214:215], v[216:217], v[214:215]
	v_pk_mul_f32 v[210:211], v[210:211], v[212:213]
	v_exp_f32_e32 v206, v206
	v_exp_f32_e32 v207, v207
	v_exp_f32_e32 v210, v210
	v_exp_f32_e32 v212, v214
	v_exp_f32_e32 v213, v215
	v_exp_f32_e32 v211, v211
	v_pk_add_f32 v[204:205], v[204:205], 1.0 op_sel_hi:[1,0]
	v_pk_add_f32 v[206:207], v[206:207], 1.0 op_sel_hi:[1,0]
	v_rcp_f32_e32 v204, v204
	v_rcp_f32_e32 v205, v205
	v_pk_add_f32 v[212:213], v[212:213], 1.0 op_sel_hi:[1,0]
	v_pk_add_f32 v[210:211], v[210:211], 1.0 op_sel_hi:[1,0]
	v_rcp_f32_e32 v206, v206
	v_rcp_f32_e32 v207, v207
	v_cvt_pk_bf16_f32 v204, v204, v205
	v_cvt_pk_bf16_f32 v205, v206, v207
	v_rcp_f32_e32 v210, v210
	v_rcp_f32_e32 v211, v211
	v_rcp_f32_e32 v212, v212
	v_rcp_f32_e32 v213, v213
	v_cvt_pk_bf16_f32 v206, v210, v211
	v_cvt_pk_bf16_f32 v207, v212, v213
	global_store_dwordx4 v[208:209], v[204:207], off offset:256 nt
	v_mul_f32_e32 v210, 0xbfb8aa3b, v187
	v_pk_mul_f32 v[212:213], v[116:117], v[210:211] op_sel_hi:[1,0]
	v_mad_i64_i32 v[204:205], s[0:1], v201, s62, v[192:193]
	v_lshl_add_u64 v[208:209], v[204:205], 0, v[194:195]
	v_cvt_f32_i32_e32 v205, v75
	v_cvt_f32_i32_e32 v207, v77
	v_cvt_f32_i32_e32 v206, v76
	v_cvt_f32_i32_e32 v204, v74
	v_pk_mul_f32 v[214:215], v[114:115], v[210:211] op_sel_hi:[1,0]
	v_pk_mul_f32 v[216:217], v[120:121], v[210:211] op_sel_hi:[1,0]
	v_pk_mul_f32 v[206:207], v[212:213], v[206:207]
	v_pk_mul_f32 v[204:205], v[214:215], v[204:205]
	v_cvt_f32_i32_e32 v213, v83
	v_cvt_f32_i32_e32 v215, v85
	v_cvt_f32_i32_e32 v214, v84
	v_cvt_f32_i32_e32 v212, v82
	v_pk_mul_f32 v[218:219], v[118:119], v[210:211] op_sel_hi:[1,0]
	v_exp_f32_e32 v204, v204
	v_pk_mul_f32 v[214:215], v[216:217], v[214:215]
	v_pk_mul_f32 v[212:213], v[218:219], v[212:213]
	v_exp_f32_e32 v205, v205
	v_exp_f32_e32 v206, v206
	v_exp_f32_e32 v207, v207
	v_exp_f32_e32 v212, v212
	v_exp_f32_e32 v214, v214
	v_exp_f32_e32 v215, v215
	v_exp_f32_e32 v213, v213
	v_pk_add_f32 v[206:207], v[206:207], 1.0 op_sel_hi:[1,0]
	v_pk_add_f32 v[204:205], v[204:205], 1.0 op_sel_hi:[1,0]
	v_pk_add_f32 v[214:215], v[214:215], 1.0 op_sel_hi:[1,0]
	v_pk_add_f32 v[212:213], v[212:213], 1.0 op_sel_hi:[1,0]
	v_rcp_f32_e32 v204, v204
	v_rcp_f32_e32 v205, v205
	v_rcp_f32_e32 v206, v206
	v_rcp_f32_e32 v207, v207
	v_rcp_f32_e32 v211, v212
	v_rcp_f32_e32 v212, v213
	v_rcp_f32_e32 v213, v214
	v_rcp_f32_e32 v214, v215
	v_cvt_pk_bf16_f32 v204, v204, v205
	v_cvt_pk_bf16_f32 v205, v206, v207
	v_cvt_pk_bf16_f32 v206, v211, v212
	v_cvt_pk_bf16_f32 v207, v213, v214
	global_store_dwordx4 v[208:209], v[204:207], off nt
	v_pk_mul_f32 v[212:213], v[108:109], v[210:211] op_sel_hi:[1,0]
	v_pk_mul_f32 v[214:215], v[106:107], v[210:211] op_sel_hi:[1,0]
	v_cvt_f32_i32_e32 v205, v59
	v_cvt_f32_i32_e32 v207, v61
	v_cvt_f32_i32_e32 v206, v60
	v_cvt_f32_i32_e32 v204, v58
	v_pk_mul_f32 v[216:217], v[112:113], v[210:211] op_sel_hi:[1,0]
	v_pk_mul_f32 v[210:211], v[110:111], v[210:211] op_sel_hi:[1,0]
	v_pk_mul_f32 v[206:207], v[212:213], v[206:207]
	v_pk_mul_f32 v[204:205], v[214:215], v[204:205]
	v_cvt_f32_i32_e32 v213, v71
	v_cvt_f32_i32_e32 v215, v73
	v_cvt_f32_i32_e32 v214, v72
	v_cvt_f32_i32_e32 v212, v70
	v_exp_f32_e32 v204, v204
	v_exp_f32_e32 v205, v205
	v_pk_mul_f32 v[214:215], v[216:217], v[214:215]
	v_pk_mul_f32 v[210:211], v[210:211], v[212:213]
	v_exp_f32_e32 v206, v206
	v_exp_f32_e32 v207, v207
	v_exp_f32_e32 v210, v210
	v_exp_f32_e32 v212, v214
	v_exp_f32_e32 v213, v215
	v_exp_f32_e32 v211, v211
	v_pk_add_f32 v[204:205], v[204:205], 1.0 op_sel_hi:[1,0]
	v_pk_add_f32 v[206:207], v[206:207], 1.0 op_sel_hi:[1,0]
	v_rcp_f32_e32 v204, v204
	v_pk_add_f32 v[212:213], v[212:213], 1.0 op_sel_hi:[1,0]
	v_pk_add_f32 v[210:211], v[210:211], 1.0 op_sel_hi:[1,0]
	v_rcp_f32_e32 v205, v205
	v_rcp_f32_e32 v206, v206
	v_rcp_f32_e32 v207, v207
	v_cvt_pk_bf16_f32 v204, v204, v205
	v_rcp_f32_e32 v210, v210
	v_rcp_f32_e32 v211, v211
	v_rcp_f32_e32 v212, v212
	v_rcp_f32_e32 v213, v213
	v_cvt_pk_bf16_f32 v205, v206, v207
	v_cvt_pk_bf16_f32 v206, v210, v211
	v_cvt_pk_bf16_f32 v207, v212, v213
	global_store_dwordx4 v[208:209], v[204:207], off offset:256 nt
	v_mul_f32_e32 v210, 0xbfb8aa3b, v184
	v_pk_mul_f32 v[212:213], v[116:117], v[210:211] op_sel_hi:[1,0]
	v_add_u32_e32 v204, 0x80, v146
	v_mad_i64_i32 v[204:205], s[0:1], v204, s62, v[192:193]
	v_lshl_add_u64 v[208:209], v[204:205], 0, v[194:195]
	v_cvt_f32_i32_e32 v205, v55
	v_cvt_f32_i32_e32 v207, v57
	v_cvt_f32_i32_e32 v206, v56
	v_cvt_f32_i32_e32 v204, v54
	v_pk_mul_f32 v[214:215], v[114:115], v[210:211] op_sel_hi:[1,0]
	v_pk_mul_f32 v[216:217], v[120:121], v[210:211] op_sel_hi:[1,0]
	v_pk_mul_f32 v[206:207], v[212:213], v[206:207]
	v_pk_mul_f32 v[204:205], v[214:215], v[204:205]
	v_cvt_f32_i32_e32 v213, v51
	v_cvt_f32_i32_e32 v215, v53
	v_cvt_f32_i32_e32 v214, v52
	v_cvt_f32_i32_e32 v212, v50
	v_pk_mul_f32 v[218:219], v[118:119], v[210:211] op_sel_hi:[1,0]
	v_exp_f32_e32 v204, v204
	v_pk_mul_f32 v[214:215], v[216:217], v[214:215]
	v_pk_mul_f32 v[212:213], v[218:219], v[212:213]
	v_exp_f32_e32 v205, v205
	v_exp_f32_e32 v206, v206
	v_exp_f32_e32 v207, v207
	v_exp_f32_e32 v212, v212
	v_exp_f32_e32 v214, v214
	v_exp_f32_e32 v215, v215
	v_exp_f32_e32 v213, v213
	v_pk_add_f32 v[206:207], v[206:207], 1.0 op_sel_hi:[1,0]
	v_pk_add_f32 v[204:205], v[204:205], 1.0 op_sel_hi:[1,0]
	v_pk_add_f32 v[214:215], v[214:215], 1.0 op_sel_hi:[1,0]
	v_pk_add_f32 v[212:213], v[212:213], 1.0 op_sel_hi:[1,0]
	v_rcp_f32_e32 v204, v204
	v_rcp_f32_e32 v205, v205
	v_rcp_f32_e32 v206, v206
	v_rcp_f32_e32 v207, v207
	v_rcp_f32_e32 v211, v212
	v_rcp_f32_e32 v212, v213
	v_rcp_f32_e32 v213, v214
	v_rcp_f32_e32 v214, v215
	v_cvt_pk_bf16_f32 v204, v204, v205
	v_cvt_pk_bf16_f32 v205, v206, v207
	v_cvt_pk_bf16_f32 v206, v211, v212
	v_cvt_pk_bf16_f32 v207, v213, v214
	global_store_dwordx4 v[208:209], v[204:207], off nt
	v_pk_mul_f32 v[212:213], v[108:109], v[210:211] op_sel_hi:[1,0]
	v_pk_mul_f32 v[214:215], v[106:107], v[210:211] op_sel_hi:[1,0]
	v_cvt_f32_i32_e32 v205, v67
	v_cvt_f32_i32_e32 v207, v69
	v_cvt_f32_i32_e32 v206, v68
	v_cvt_f32_i32_e32 v204, v66
	v_pk_mul_f32 v[216:217], v[112:113], v[210:211] op_sel_hi:[1,0]
	v_pk_mul_f32 v[210:211], v[110:111], v[210:211] op_sel_hi:[1,0]
	v_pk_mul_f32 v[206:207], v[212:213], v[206:207]
	v_pk_mul_f32 v[204:205], v[214:215], v[204:205]
	v_cvt_f32_i32_e32 v213, v63
	v_cvt_f32_i32_e32 v215, v65
	v_cvt_f32_i32_e32 v214, v64
	v_cvt_f32_i32_e32 v212, v62
	v_exp_f32_e32 v204, v204
	v_exp_f32_e32 v205, v205
	v_pk_mul_f32 v[214:215], v[216:217], v[214:215]
	v_pk_mul_f32 v[210:211], v[210:211], v[212:213]
	v_exp_f32_e32 v206, v206
	v_exp_f32_e32 v207, v207
	v_exp_f32_e32 v210, v210
	v_exp_f32_e32 v212, v214
	v_exp_f32_e32 v213, v215
	v_exp_f32_e32 v211, v211
	v_pk_add_f32 v[204:205], v[204:205], 1.0 op_sel_hi:[1,0]
	v_pk_add_f32 v[206:207], v[206:207], 1.0 op_sel_hi:[1,0]
	v_rcp_f32_e32 v204, v204
	v_pk_add_f32 v[212:213], v[212:213], 1.0 op_sel_hi:[1,0]
	v_pk_add_f32 v[210:211], v[210:211], 1.0 op_sel_hi:[1,0]
	v_rcp_f32_e32 v205, v205
	v_rcp_f32_e32 v206, v206
	v_rcp_f32_e32 v207, v207
	v_cvt_pk_bf16_f32 v204, v204, v205
	v_rcp_f32_e32 v210, v210
	v_rcp_f32_e32 v211, v211
	v_rcp_f32_e32 v212, v212
	v_rcp_f32_e32 v213, v213
	v_cvt_pk_bf16_f32 v205, v206, v207
	v_cvt_pk_bf16_f32 v206, v210, v211
	v_cvt_pk_bf16_f32 v207, v212, v213
	global_store_dwordx4 v[208:209], v[204:207], off offset:256 nt
	v_mul_f32_e32 v210, 0xbfb8aa3b, v185
	v_pk_mul_f32 v[212:213], v[116:117], v[210:211] op_sel_hi:[1,0]
	v_add_u32_e32 v204, 0x90, v146
	v_mad_i64_i32 v[204:205], s[0:1], v204, s62, v[192:193]
	v_lshl_add_u64 v[208:209], v[204:205], 0, v[194:195]
	v_cvt_f32_i32_e32 v205, v35
	v_cvt_f32_i32_e32 v207, v37
	v_cvt_f32_i32_e32 v206, v36
	v_cvt_f32_i32_e32 v204, v34
	v_pk_mul_f32 v[214:215], v[114:115], v[210:211] op_sel_hi:[1,0]
	v_pk_mul_f32 v[216:217], v[120:121], v[210:211] op_sel_hi:[1,0]
	v_pk_mul_f32 v[206:207], v[212:213], v[206:207]
	v_pk_mul_f32 v[204:205], v[214:215], v[204:205]
	v_cvt_f32_i32_e32 v213, v39
	v_cvt_f32_i32_e32 v215, v41
	v_cvt_f32_i32_e32 v214, v40
	v_cvt_f32_i32_e32 v212, v38
	v_pk_mul_f32 v[218:219], v[118:119], v[210:211] op_sel_hi:[1,0]
	v_exp_f32_e32 v204, v204
	v_pk_mul_f32 v[214:215], v[216:217], v[214:215]
	v_pk_mul_f32 v[212:213], v[218:219], v[212:213]
	v_exp_f32_e32 v205, v205
	v_exp_f32_e32 v206, v206
	v_exp_f32_e32 v207, v207
	v_exp_f32_e32 v212, v212
	v_exp_f32_e32 v214, v214
	v_exp_f32_e32 v215, v215
	v_exp_f32_e32 v213, v213
	v_pk_add_f32 v[206:207], v[206:207], 1.0 op_sel_hi:[1,0]
	v_pk_add_f32 v[204:205], v[204:205], 1.0 op_sel_hi:[1,0]
	v_pk_add_f32 v[214:215], v[214:215], 1.0 op_sel_hi:[1,0]
	v_pk_add_f32 v[212:213], v[212:213], 1.0 op_sel_hi:[1,0]
	v_rcp_f32_e32 v204, v204
	v_rcp_f32_e32 v205, v205
	v_rcp_f32_e32 v206, v206
	v_rcp_f32_e32 v207, v207
	v_rcp_f32_e32 v211, v212
	v_rcp_f32_e32 v212, v213
	v_rcp_f32_e32 v213, v214
	v_rcp_f32_e32 v214, v215
	v_cvt_pk_bf16_f32 v204, v204, v205
	v_cvt_pk_bf16_f32 v205, v206, v207
	v_cvt_pk_bf16_f32 v206, v211, v212
	v_cvt_pk_bf16_f32 v207, v213, v214
	global_store_dwordx4 v[208:209], v[204:207], off nt
	v_pk_mul_f32 v[212:213], v[108:109], v[210:211] op_sel_hi:[1,0]
	v_pk_mul_f32 v[214:215], v[106:107], v[210:211] op_sel_hi:[1,0]
	v_cvt_f32_i32_e32 v205, v43
	v_cvt_f32_i32_e32 v207, v45
	v_cvt_f32_i32_e32 v206, v44
	v_cvt_f32_i32_e32 v204, v42
	v_pk_mul_f32 v[216:217], v[112:113], v[210:211] op_sel_hi:[1,0]
	v_pk_mul_f32 v[210:211], v[110:111], v[210:211] op_sel_hi:[1,0]
	v_pk_mul_f32 v[206:207], v[212:213], v[206:207]
	v_pk_mul_f32 v[204:205], v[214:215], v[204:205]
	v_cvt_f32_i32_e32 v213, v47
	v_cvt_f32_i32_e32 v215, v49
	v_cvt_f32_i32_e32 v214, v48
	v_cvt_f32_i32_e32 v212, v46
	v_exp_f32_e32 v204, v204
	v_exp_f32_e32 v205, v205
	v_pk_mul_f32 v[214:215], v[216:217], v[214:215]
	v_pk_mul_f32 v[210:211], v[210:211], v[212:213]
	v_exp_f32_e32 v206, v206
	v_exp_f32_e32 v207, v207
	v_exp_f32_e32 v210, v210
	v_exp_f32_e32 v212, v214
	v_exp_f32_e32 v213, v215
	v_exp_f32_e32 v211, v211
	v_pk_add_f32 v[204:205], v[204:205], 1.0 op_sel_hi:[1,0]
	v_pk_add_f32 v[206:207], v[206:207], 1.0 op_sel_hi:[1,0]
	v_rcp_f32_e32 v204, v204
	v_pk_add_f32 v[212:213], v[212:213], 1.0 op_sel_hi:[1,0]
	v_pk_add_f32 v[210:211], v[210:211], 1.0 op_sel_hi:[1,0]
	v_rcp_f32_e32 v205, v205
	v_rcp_f32_e32 v206, v206
	v_rcp_f32_e32 v207, v207
	v_cvt_pk_bf16_f32 v204, v204, v205
	v_rcp_f32_e32 v210, v210
	v_rcp_f32_e32 v211, v211
	v_rcp_f32_e32 v212, v212
	v_rcp_f32_e32 v213, v213
	v_cvt_pk_bf16_f32 v205, v206, v207
	v_cvt_pk_bf16_f32 v206, v210, v211
	v_cvt_pk_bf16_f32 v207, v212, v213
	global_store_dwordx4 v[208:209], v[204:207], off offset:256 nt
	v_mul_f32_e32 v210, 0xbfb8aa3b, v182
	v_pk_mul_f32 v[212:213], v[116:117], v[210:211] op_sel_hi:[1,0]
	v_add_u32_e32 v204, 0xa0, v146
	v_mad_i64_i32 v[204:205], s[0:1], v204, s62, v[192:193]
	v_lshl_add_u64 v[208:209], v[204:205], 0, v[194:195]
	v_cvt_f32_i32_e32 v205, v23
	v_cvt_f32_i32_e32 v207, v25
	v_cvt_f32_i32_e32 v206, v24
	v_cvt_f32_i32_e32 v204, v22
	v_pk_mul_f32 v[214:215], v[114:115], v[210:211] op_sel_hi:[1,0]
	v_pk_mul_f32 v[216:217], v[120:121], v[210:211] op_sel_hi:[1,0]
	v_pk_mul_f32 v[206:207], v[212:213], v[206:207]
	v_pk_mul_f32 v[204:205], v[214:215], v[204:205]
	v_cvt_f32_i32_e32 v213, v19
	v_cvt_f32_i32_e32 v215, v21
	v_cvt_f32_i32_e32 v214, v20
	v_cvt_f32_i32_e32 v212, v18
	v_pk_mul_f32 v[218:219], v[118:119], v[210:211] op_sel_hi:[1,0]
	v_exp_f32_e32 v204, v204
	v_pk_mul_f32 v[214:215], v[216:217], v[214:215]
	v_pk_mul_f32 v[212:213], v[218:219], v[212:213]
	v_exp_f32_e32 v205, v205
	v_exp_f32_e32 v206, v206
	v_exp_f32_e32 v207, v207
	v_exp_f32_e32 v212, v212
	v_exp_f32_e32 v214, v214
	v_exp_f32_e32 v215, v215
	v_exp_f32_e32 v213, v213
	v_pk_add_f32 v[206:207], v[206:207], 1.0 op_sel_hi:[1,0]
	v_pk_add_f32 v[204:205], v[204:205], 1.0 op_sel_hi:[1,0]
	v_pk_add_f32 v[214:215], v[214:215], 1.0 op_sel_hi:[1,0]
	v_pk_add_f32 v[212:213], v[212:213], 1.0 op_sel_hi:[1,0]
	v_rcp_f32_e32 v204, v204
	v_rcp_f32_e32 v205, v205
	v_rcp_f32_e32 v206, v206
	v_rcp_f32_e32 v207, v207
	v_rcp_f32_e32 v211, v212
	v_rcp_f32_e32 v212, v213
	v_rcp_f32_e32 v213, v214
	v_rcp_f32_e32 v214, v215
	v_cvt_pk_bf16_f32 v204, v204, v205
	v_cvt_pk_bf16_f32 v205, v206, v207
	v_cvt_pk_bf16_f32 v206, v211, v212
	v_cvt_pk_bf16_f32 v207, v213, v214
	global_store_dwordx4 v[208:209], v[204:207], off nt
	v_pk_mul_f32 v[212:213], v[108:109], v[210:211] op_sel_hi:[1,0]
	v_pk_mul_f32 v[214:215], v[106:107], v[210:211] op_sel_hi:[1,0]
	v_cvt_f32_i32_e32 v205, v31
	v_cvt_f32_i32_e32 v207, v33
	v_cvt_f32_i32_e32 v206, v32
	v_cvt_f32_i32_e32 v204, v30
	v_pk_mul_f32 v[216:217], v[112:113], v[210:211] op_sel_hi:[1,0]
	v_pk_mul_f32 v[210:211], v[110:111], v[210:211] op_sel_hi:[1,0]
	v_pk_mul_f32 v[206:207], v[212:213], v[206:207]
	v_pk_mul_f32 v[204:205], v[214:215], v[204:205]
	v_cvt_f32_i32_e32 v213, v27
	v_cvt_f32_i32_e32 v215, v29
	v_cvt_f32_i32_e32 v214, v28
	v_cvt_f32_i32_e32 v212, v26
	v_exp_f32_e32 v204, v204
	v_exp_f32_e32 v205, v205
	v_pk_mul_f32 v[214:215], v[216:217], v[214:215]
	v_pk_mul_f32 v[210:211], v[210:211], v[212:213]
	v_exp_f32_e32 v206, v206
	v_exp_f32_e32 v207, v207
	v_exp_f32_e32 v210, v210
	v_exp_f32_e32 v212, v214
	v_exp_f32_e32 v213, v215
	v_exp_f32_e32 v211, v211
	v_pk_add_f32 v[204:205], v[204:205], 1.0 op_sel_hi:[1,0]
	v_pk_add_f32 v[206:207], v[206:207], 1.0 op_sel_hi:[1,0]
	v_rcp_f32_e32 v204, v204
	v_pk_add_f32 v[212:213], v[212:213], 1.0 op_sel_hi:[1,0]
	v_pk_add_f32 v[210:211], v[210:211], 1.0 op_sel_hi:[1,0]
	v_rcp_f32_e32 v205, v205
	v_rcp_f32_e32 v206, v206
	v_rcp_f32_e32 v207, v207
	v_cvt_pk_bf16_f32 v204, v204, v205
	v_rcp_f32_e32 v210, v210
	v_rcp_f32_e32 v211, v211
	v_rcp_f32_e32 v212, v212
	v_rcp_f32_e32 v213, v213
	v_cvt_pk_bf16_f32 v205, v206, v207
	v_cvt_pk_bf16_f32 v206, v210, v211
	v_cvt_pk_bf16_f32 v207, v212, v213
	global_store_dwordx4 v[208:209], v[204:207], off offset:256 nt
	s_nop 1
	v_add_u32_e32 v204, 0xb0, v146
	v_mad_i64_i32 v[192:193], s[0:1], v204, s62, v[192:193]
	v_lshl_add_u64 v[204:205], v[192:193], 0, v[194:195]
	v_cvt_f32_i32_e32 v193, v3
	v_cvt_f32_i32_e32 v195, v5
	v_cvt_f32_i32_e32 v194, v4
	v_cvt_f32_i32_e32 v192, v2
	v_mul_f32_e32 v206, 0xbfb8aa3b, v183
	v_pk_mul_f32 v[208:209], v[116:117], v[206:207] op_sel_hi:[1,0]
	v_pk_mul_f32 v[210:211], v[114:115], v[206:207] op_sel_hi:[1,0]
	v_pk_mul_f32 v[194:195], v[208:209], v[194:195]
	v_pk_mul_f32 v[192:193], v[210:211], v[192:193]
	v_cvt_f32_i32_e32 v209, v7
	v_cvt_f32_i32_e32 v211, v9
	v_cvt_f32_i32_e32 v210, v8
	v_cvt_f32_i32_e32 v208, v6
	v_pk_mul_f32 v[212:213], v[120:121], v[206:207] op_sel_hi:[1,0]
	v_pk_mul_f32 v[214:215], v[118:119], v[206:207] op_sel_hi:[1,0]
	v_pk_mul_f32 v[210:211], v[212:213], v[210:211]
	v_pk_mul_f32 v[208:209], v[214:215], v[208:209]
	v_exp_f32_e32 v192, v192
	v_exp_f32_e32 v193, v193
	v_exp_f32_e32 v194, v194
	v_exp_f32_e32 v195, v195
	v_exp_f32_e32 v208, v208
	v_exp_f32_e32 v210, v210
	v_exp_f32_e32 v211, v211
	v_exp_f32_e32 v209, v209
	v_pk_add_f32 v[194:195], v[194:195], 1.0 op_sel_hi:[1,0]
	v_pk_add_f32 v[192:193], v[192:193], 1.0 op_sel_hi:[1,0]
	v_pk_add_f32 v[210:211], v[210:211], 1.0 op_sel_hi:[1,0]
	v_pk_add_f32 v[208:209], v[208:209], 1.0 op_sel_hi:[1,0]
	v_rcp_f32_e32 v192, v192
	v_rcp_f32_e32 v193, v193
	v_rcp_f32_e32 v194, v194
	v_rcp_f32_e32 v195, v195
	v_rcp_f32_e32 v207, v208
	v_rcp_f32_e32 v208, v209
	v_rcp_f32_e32 v209, v210
	v_rcp_f32_e32 v210, v211
	v_cvt_pk_bf16_f32 v192, v192, v193
	v_cvt_pk_bf16_f32 v193, v194, v195
	v_cvt_pk_bf16_f32 v194, v207, v208
	v_cvt_pk_bf16_f32 v195, v209, v210
	global_store_dwordx4 v[204:205], v[192:195], off nt
	v_pk_mul_f32 v[208:209], v[108:109], v[206:207] op_sel_hi:[1,0]
	v_pk_mul_f32 v[210:211], v[106:107], v[206:207] op_sel_hi:[1,0]
	v_cvt_f32_i32_e32 v193, v11
	v_cvt_f32_i32_e32 v195, v13
	v_cvt_f32_i32_e32 v194, v12
	v_cvt_f32_i32_e32 v192, v10
	v_pk_mul_f32 v[212:213], v[112:113], v[206:207] op_sel_hi:[1,0]
	v_pk_mul_f32 v[206:207], v[110:111], v[206:207] op_sel_hi:[1,0]
	v_pk_mul_f32 v[194:195], v[208:209], v[194:195]
	v_pk_mul_f32 v[192:193], v[210:211], v[192:193]
	v_cvt_f32_i32_e32 v209, v15
	v_cvt_f32_i32_e32 v211, v17
	v_cvt_f32_i32_e32 v210, v16
	v_cvt_f32_i32_e32 v208, v14
	v_exp_f32_e32 v192, v192
	v_exp_f32_e32 v193, v193
	v_pk_mul_f32 v[210:211], v[212:213], v[210:211]
	v_pk_mul_f32 v[206:207], v[206:207], v[208:209]
	v_exp_f32_e32 v194, v194
	v_exp_f32_e32 v195, v195
	v_exp_f32_e32 v206, v206
	v_exp_f32_e32 v208, v210
	v_exp_f32_e32 v209, v211
	v_exp_f32_e32 v207, v207
	v_pk_add_f32 v[194:195], v[194:195], 1.0 op_sel_hi:[1,0]
	v_pk_add_f32 v[192:193], v[192:193], 1.0 op_sel_hi:[1,0]
	v_pk_add_f32 v[208:209], v[208:209], 1.0 op_sel_hi:[1,0]
	v_pk_add_f32 v[206:207], v[206:207], 1.0 op_sel_hi:[1,0]
	v_rcp_f32_e32 v192, v192
	v_rcp_f32_e32 v193, v193
	v_rcp_f32_e32 v194, v194
	v_rcp_f32_e32 v195, v195
	v_rcp_f32_e32 v206, v206
	v_rcp_f32_e32 v207, v207
	v_rcp_f32_e32 v208, v208
	v_rcp_f32_e32 v209, v209
	v_cvt_pk_bf16_f32 v192, v192, v193
	v_cvt_pk_bf16_f32 v193, v194, v195
	v_cvt_pk_bf16_f32 v194, v206, v207
	v_cvt_pk_bf16_f32 v195, v208, v209
	global_store_dwordx4 v[204:205], v[192:195], off offset:256 nt
	s_mov_b64 s[0:1], 0

.LBB0_255:
	s_lshl_b32 s1, s1, 11
	s_and_b32 s1, s1, 0x800
	s_add_i32 s1, s1, 0
	s_lshl_b32 s11, s0, 8
	s_add_i32 s1, s1, 0x25500
	s_add_i32 s11, s11, s54
	s_cmp_lt_i32 s10, 44
	s_cselect_b32 s0, 1, 2
	s_lshl_b32 s4, s20, 2
	s_add_i32 s4, s1, s4
	v_lshl_add_u32 v110, v160, 2, s4
	s_lshl_b32 s4, s54, 2
	s_add_i32 s1, s1, s4
	v_lshl_add_u32 v146, v167, 2, s1
	ds_read_b128 v[114:117], v110 offset:1024
	ds_read_b128 v[118:121], v110 offset:1040
	ds_read_b128 v[106:109], v110 offset:1536
	ds_read_b128 v[110:113], v110 offset:1552
	ds_read2_b32 v[188:189], v146 offset1:16
	ds_read2_b32 v[186:187], v146 offset0:32 offset1:48
	ds_read2_b32 v[184:185], v146 offset0:128 offset1:144
	ds_read2_b32 v[182:183], v146 offset0:160 offset1:176
	s_cmp_gt_i32 s10, 35
	s_cselect_b32 s4, s0, 0
	v_or_b32_e32 v146, s11, v167
	s_cmp_lt_i32 s4, 1
	s_mov_b64 s[0:1], -1
	s_cbranch_scc1 .LBB0_262
	v_lshl_or_b32 v190, s10, 8, v197
	s_cmp_lg_u32 s4, 1
	v_ashrrev_i32_e32 v191, 31, v190
	v_or_b32_e32 v203, 16, v146
	v_or_b32_e32 v202, 32, v146
	v_or_b32_e32 v201, 48, v146
	s_cbranch_scc0 .LBB0_258
	v_mov_b64_e32 v[192:193], s[88:89]
	v_mad_i64_i32 v[204:205], s[0:1], v146, s58, v[192:193]
	v_lshlrev_b64 v[194:195], 1, v[190:191]
	v_lshl_add_u64 v[208:209], v[204:205], 0, v[194:195]
	v_cvt_f32_i32_e32 v205, v143
	v_cvt_f32_i32_e32 v207, v145
	v_cvt_f32_i32_e32 v206, v144
	v_cvt_f32_i32_e32 v204, v142
	s_waitcnt lgkmcnt(0)
	v_mul_f32_e32 v210, 0xbfb8aa3b, v188
	v_pk_mul_f32 v[212:213], v[116:117], v[210:211] op_sel_hi:[1,0]
	v_pk_mul_f32 v[214:215], v[114:115], v[210:211] op_sel_hi:[1,0]
	v_pk_mul_f32 v[206:207], v[212:213], v[206:207]
	v_pk_mul_f32 v[204:205], v[214:215], v[204:205]
	v_cvt_f32_i32_e32 v213, v139
	v_cvt_f32_i32_e32 v215, v141
	v_cvt_f32_i32_e32 v214, v140
	v_cvt_f32_i32_e32 v212, v138
	v_pk_mul_f32 v[216:217], v[120:121], v[210:211] op_sel_hi:[1,0]
	v_pk_mul_f32 v[218:219], v[118:119], v[210:211] op_sel_hi:[1,0]
	v_pk_mul_f32 v[214:215], v[216:217], v[214:215]
	v_pk_mul_f32 v[212:213], v[218:219], v[212:213]
	v_exp_f32_e32 v204, v204
	v_exp_f32_e32 v205, v205
	v_exp_f32_e32 v206, v206
	v_exp_f32_e32 v207, v207
	v_exp_f32_e32 v212, v212
	v_exp_f32_e32 v214, v214
	v_exp_f32_e32 v215, v215
	v_exp_f32_e32 v213, v213
	v_pk_add_f32 v[206:207], v[206:207], 1.0 op_sel_hi:[1,0]
	v_pk_add_f32 v[204:205], v[204:205], 1.0 op_sel_hi:[1,0]
	v_pk_add_f32 v[214:215], v[214:215], 1.0 op_sel_hi:[1,0]
	v_pk_add_f32 v[212:213], v[212:213], 1.0 op_sel_hi:[1,0]
	v_rcp_f32_e32 v204, v204
	v_rcp_f32_e32 v205, v205
	v_rcp_f32_e32 v206, v206
	v_rcp_f32_e32 v207, v207
	v_rcp_f32_e32 v211, v212
	v_rcp_f32_e32 v212, v213
	v_rcp_f32_e32 v213, v214
	v_rcp_f32_e32 v214, v215
	v_cvt_pk_bf16_f32 v204, v204, v205
	v_cvt_pk_bf16_f32 v205, v206, v207
	v_cvt_pk_bf16_f32 v206, v211, v212
	v_cvt_pk_bf16_f32 v207, v213, v214
	global_store_dwordx4 v[208:209], v[204:207], off nt
	v_pk_mul_f32 v[212:213], v[108:109], v[210:211] op_sel_hi:[1,0]
	v_pk_mul_f32 v[214:215], v[106:107], v[210:211] op_sel_hi:[1,0]
	v_cvt_f32_i32_e32 v205, v135
	v_cvt_f32_i32_e32 v207, v137
	v_cvt_f32_i32_e32 v206, v136
	v_cvt_f32_i32_e32 v204, v134
	v_pk_mul_f32 v[216:217], v[112:113], v[210:211] op_sel_hi:[1,0]
	v_pk_mul_f32 v[210:211], v[110:111], v[210:211] op_sel_hi:[1,0]
	v_pk_mul_f32 v[206:207], v[212:213], v[206:207]
	v_pk_mul_f32 v[204:205], v[214:215], v[204:205]
	v_cvt_f32_i32_e32 v213, v131
	v_cvt_f32_i32_e32 v215, v133
	v_cvt_f32_i32_e32 v214, v132
	v_cvt_f32_i32_e32 v212, v130
	v_exp_f32_e32 v204, v204
	v_exp_f32_e32 v205, v205
	v_pk_mul_f32 v[214:215], v[216:217], v[214:215]
	v_pk_mul_f32 v[210:211], v[210:211], v[212:213]
	v_exp_f32_e32 v206, v206
	v_exp_f32_e32 v207, v207
	v_exp_f32_e32 v210, v210
	v_exp_f32_e32 v212, v214
	v_exp_f32_e32 v213, v215
	v_exp_f32_e32 v211, v211
	v_pk_add_f32 v[204:205], v[204:205], 1.0 op_sel_hi:[1,0]
	v_pk_add_f32 v[206:207], v[206:207], 1.0 op_sel_hi:[1,0]
	v_rcp_f32_e32 v204, v204
	v_rcp_f32_e32 v205, v205
	v_pk_add_f32 v[212:213], v[212:213], 1.0 op_sel_hi:[1,0]
	v_pk_add_f32 v[210:211], v[210:211], 1.0 op_sel_hi:[1,0]
	v_rcp_f32_e32 v206, v206
	v_rcp_f32_e32 v207, v207
	v_cvt_pk_bf16_f32 v204, v204, v205
	v_cvt_pk_bf16_f32 v205, v206, v207
	v_rcp_f32_e32 v210, v210
	v_rcp_f32_e32 v211, v211
	v_rcp_f32_e32 v212, v212
	v_rcp_f32_e32 v213, v213
	v_cvt_pk_bf16_f32 v206, v210, v211
	v_cvt_pk_bf16_f32 v207, v212, v213
	global_store_dwordx4 v[208:209], v[204:207], off offset:256 nt
	v_mul_f32_e32 v210, 0xbfb8aa3b, v189
	v_pk_mul_f32 v[212:213], v[116:117], v[210:211] op_sel_hi:[1,0]
	v_mad_i64_i32 v[204:205], s[0:1], v203, s58, v[192:193]
	v_lshl_add_u64 v[208:209], v[204:205], 0, v[194:195]
	v_cvt_f32_i32_e32 v205, v123
	v_cvt_f32_i32_e32 v207, v125
	v_cvt_f32_i32_e32 v206, v124
	v_cvt_f32_i32_e32 v204, v122
	v_pk_mul_f32 v[214:215], v[114:115], v[210:211] op_sel_hi:[1,0]
	v_pk_mul_f32 v[216:217], v[120:121], v[210:211] op_sel_hi:[1,0]
	v_pk_mul_f32 v[206:207], v[212:213], v[206:207]
	v_pk_mul_f32 v[204:205], v[214:215], v[204:205]
	v_cvt_f32_i32_e32 v213, v127
	v_cvt_f32_i32_e32 v215, v129
	v_cvt_f32_i32_e32 v214, v128
	v_cvt_f32_i32_e32 v212, v126
	v_pk_mul_f32 v[218:219], v[118:119], v[210:211] op_sel_hi:[1,0]
	v_exp_f32_e32 v204, v204
	v_pk_mul_f32 v[214:215], v[216:217], v[214:215]
	v_pk_mul_f32 v[212:213], v[218:219], v[212:213]
	v_exp_f32_e32 v205, v205
	v_exp_f32_e32 v206, v206
	v_exp_f32_e32 v207, v207
	v_exp_f32_e32 v212, v212
	v_exp_f32_e32 v214, v214
	v_exp_f32_e32 v215, v215
	v_exp_f32_e32 v213, v213
	v_pk_add_f32 v[206:207], v[206:207], 1.0 op_sel_hi:[1,0]
	v_pk_add_f32 v[204:205], v[204:205], 1.0 op_sel_hi:[1,0]
	v_pk_add_f32 v[214:215], v[214:215], 1.0 op_sel_hi:[1,0]
	v_pk_add_f32 v[212:213], v[212:213], 1.0 op_sel_hi:[1,0]
	v_rcp_f32_e32 v204, v204
	v_rcp_f32_e32 v205, v205
	v_rcp_f32_e32 v206, v206
	v_rcp_f32_e32 v207, v207
	v_rcp_f32_e32 v211, v212
	v_rcp_f32_e32 v212, v213
	v_rcp_f32_e32 v213, v214
	v_rcp_f32_e32 v214, v215
	v_cvt_pk_bf16_f32 v204, v204, v205
	v_cvt_pk_bf16_f32 v205, v206, v207
	v_cvt_pk_bf16_f32 v206, v211, v212
	v_cvt_pk_bf16_f32 v207, v213, v214
	global_store_dwordx4 v[208:209], v[204:207], off nt
	v_pk_mul_f32 v[212:213], v[108:109], v[210:211] op_sel_hi:[1,0]
	v_pk_mul_f32 v[214:215], v[106:107], v[210:211] op_sel_hi:[1,0]
	v_cvt_f32_i32_e32 v205, v99
	v_cvt_f32_i32_e32 v207, v101
	v_cvt_f32_i32_e32 v206, v100
	v_cvt_f32_i32_e32 v204, v98
	v_pk_mul_f32 v[216:217], v[112:113], v[210:211] op_sel_hi:[1,0]
	v_pk_mul_f32 v[210:211], v[110:111], v[210:211] op_sel_hi:[1,0]
	v_pk_mul_f32 v[206:207], v[212:213], v[206:207]
	v_pk_mul_f32 v[204:205], v[214:215], v[204:205]
	v_cvt_f32_i32_e32 v213, v103
	v_cvt_f32_i32_e32 v215, v105
	v_cvt_f32_i32_e32 v214, v104
	v_cvt_f32_i32_e32 v212, v102
	v_exp_f32_e32 v204, v204
	v_exp_f32_e32 v205, v205
	v_pk_mul_f32 v[214:215], v[216:217], v[214:215]
	v_pk_mul_f32 v[210:211], v[210:211], v[212:213]
	v_exp_f32_e32 v206, v206
	v_exp_f32_e32 v207, v207
	v_exp_f32_e32 v210, v210
	v_exp_f32_e32 v212, v214
	v_exp_f32_e32 v213, v215
	v_exp_f32_e32 v211, v211
	v_pk_add_f32 v[204:205], v[204:205], 1.0 op_sel_hi:[1,0]
	v_pk_add_f32 v[206:207], v[206:207], 1.0 op_sel_hi:[1,0]
	v_rcp_f32_e32 v204, v204
	v_rcp_f32_e32 v205, v205
	v_pk_add_f32 v[212:213], v[212:213], 1.0 op_sel_hi:[1,0]
	v_pk_add_f32 v[210:211], v[210:211], 1.0 op_sel_hi:[1,0]
	v_rcp_f32_e32 v206, v206
	v_rcp_f32_e32 v207, v207
	v_cvt_pk_bf16_f32 v204, v204, v205
	v_cvt_pk_bf16_f32 v205, v206, v207
	v_rcp_f32_e32 v210, v210
	v_rcp_f32_e32 v211, v211
	v_rcp_f32_e32 v212, v212
	v_rcp_f32_e32 v213, v213
	v_cvt_pk_bf16_f32 v206, v210, v211
	v_cvt_pk_bf16_f32 v207, v212, v213
	global_store_dwordx4 v[208:209], v[204:207], off offset:256 nt
	v_mul_f32_e32 v210, 0xbfb8aa3b, v186
	v_pk_mul_f32 v[212:213], v[116:117], v[210:211] op_sel_hi:[1,0]
	v_mad_i64_i32 v[204:205], s[0:1], v202, s58, v[192:193]
	v_lshl_add_u64 v[208:209], v[204:205], 0, v[194:195]
	v_cvt_f32_i32_e32 v205, v95
	v_cvt_f32_i32_e32 v207, v97
	v_cvt_f32_i32_e32 v206, v96
	v_cvt_f32_i32_e32 v204, v94
	v_pk_mul_f32 v[214:215], v[114:115], v[210:211] op_sel_hi:[1,0]
	v_pk_mul_f32 v[216:217], v[120:121], v[210:211] op_sel_hi:[1,0]
	v_pk_mul_f32 v[206:207], v[212:213], v[206:207]
	v_pk_mul_f32 v[204:205], v[214:215], v[204:205]
	v_cvt_f32_i32_e32 v213, v91
	v_cvt_f32_i32_e32 v215, v93
	v_cvt_f32_i32_e32 v214, v92
	v_cvt_f32_i32_e32 v212, v90
	v_pk_mul_f32 v[218:219], v[118:119], v[210:211] op_sel_hi:[1,0]
	v_exp_f32_e32 v204, v204
	v_pk_mul_f32 v[214:215], v[216:217], v[214:215]
	v_pk_mul_f32 v[212:213], v[218:219], v[212:213]
	v_exp_f32_e32 v205, v205
	v_exp_f32_e32 v206, v206
	v_exp_f32_e32 v207, v207
	v_exp_f32_e32 v212, v212
	v_exp_f32_e32 v214, v214
	v_exp_f32_e32 v215, v215
	v_exp_f32_e32 v213, v213
	v_pk_add_f32 v[206:207], v[206:207], 1.0 op_sel_hi:[1,0]
	v_pk_add_f32 v[204:205], v[204:205], 1.0 op_sel_hi:[1,0]
	v_pk_add_f32 v[214:215], v[214:215], 1.0 op_sel_hi:[1,0]
	v_pk_add_f32 v[212:213], v[212:213], 1.0 op_sel_hi:[1,0]
	v_rcp_f32_e32 v204, v204
	v_rcp_f32_e32 v205, v205
	v_rcp_f32_e32 v206, v206
	v_rcp_f32_e32 v207, v207
	v_rcp_f32_e32 v211, v212
	v_rcp_f32_e32 v212, v213
	v_rcp_f32_e32 v213, v214
	v_rcp_f32_e32 v214, v215
	v_cvt_pk_bf16_f32 v204, v204, v205
	v_cvt_pk_bf16_f32 v205, v206, v207
	v_cvt_pk_bf16_f32 v206, v211, v212
	v_cvt_pk_bf16_f32 v207, v213, v214
	global_store_dwordx4 v[208:209], v[204:207], off nt
	v_pk_mul_f32 v[212:213], v[108:109], v[210:211] op_sel_hi:[1,0]
	v_pk_mul_f32 v[214:215], v[106:107], v[210:211] op_sel_hi:[1,0]
	v_cvt_f32_i32_e32 v205, v87
	v_cvt_f32_i32_e32 v207, v89
	v_cvt_f32_i32_e32 v206, v88
	v_cvt_f32_i32_e32 v204, v86
	v_pk_mul_f32 v[216:217], v[112:113], v[210:211] op_sel_hi:[1,0]
	v_pk_mul_f32 v[210:211], v[110:111], v[210:211] op_sel_hi:[1,0]
	v_pk_mul_f32 v[206:207], v[212:213], v[206:207]
	v_pk_mul_f32 v[204:205], v[214:215], v[204:205]
	v_cvt_f32_i32_e32 v213, v79
	v_cvt_f32_i32_e32 v215, v81
	v_cvt_f32_i32_e32 v214, v80
	v_cvt_f32_i32_e32 v212, v78
	v_exp_f32_e32 v204, v204
	v_exp_f32_e32 v205, v205
	v_pk_mul_f32 v[214:215], v[216:217], v[214:215]
	v_pk_mul_f32 v[210:211], v[210:211], v[212:213]
	v_exp_f32_e32 v206, v206
	v_exp_f32_e32 v207, v207
	v_exp_f32_e32 v210, v210
	v_exp_f32_e32 v212, v214
	v_exp_f32_e32 v213, v215
	v_exp_f32_e32 v211, v211
	v_pk_add_f32 v[204:205], v[204:205], 1.0 op_sel_hi:[1,0]
	v_pk_add_f32 v[206:207], v[206:207], 1.0 op_sel_hi:[1,0]
	v_rcp_f32_e32 v204, v204
	v_rcp_f32_e32 v205, v205
	v_pk_add_f32 v[212:213], v[212:213], 1.0 op_sel_hi:[1,0]
	v_pk_add_f32 v[210:211], v[210:211], 1.0 op_sel_hi:[1,0]
	v_rcp_f32_e32 v206, v206
	v_rcp_f32_e32 v207, v207
	v_cvt_pk_bf16_f32 v204, v204, v205
	v_cvt_pk_bf16_f32 v205, v206, v207
	v_rcp_f32_e32 v210, v210
	v_rcp_f32_e32 v211, v211
	v_rcp_f32_e32 v212, v212
	v_rcp_f32_e32 v213, v213
	v_cvt_pk_bf16_f32 v206, v210, v211
	v_cvt_pk_bf16_f32 v207, v212, v213
	global_store_dwordx4 v[208:209], v[204:207], off offset:256 nt
	v_mul_f32_e32 v210, 0xbfb8aa3b, v187
	v_pk_mul_f32 v[212:213], v[116:117], v[210:211] op_sel_hi:[1,0]
	v_mad_i64_i32 v[204:205], s[0:1], v201, s58, v[192:193]
	v_lshl_add_u64 v[208:209], v[204:205], 0, v[194:195]
	v_cvt_f32_i32_e32 v205, v75
	v_cvt_f32_i32_e32 v207, v77
	v_cvt_f32_i32_e32 v206, v76
	v_cvt_f32_i32_e32 v204, v74
	v_pk_mul_f32 v[214:215], v[114:115], v[210:211] op_sel_hi:[1,0]
	v_pk_mul_f32 v[216:217], v[120:121], v[210:211] op_sel_hi:[1,0]
	v_pk_mul_f32 v[206:207], v[212:213], v[206:207]
	v_pk_mul_f32 v[204:205], v[214:215], v[204:205]
	v_cvt_f32_i32_e32 v213, v83
	v_cvt_f32_i32_e32 v215, v85
	v_cvt_f32_i32_e32 v214, v84
	v_cvt_f32_i32_e32 v212, v82
	v_pk_mul_f32 v[218:219], v[118:119], v[210:211] op_sel_hi:[1,0]
	v_exp_f32_e32 v204, v204
	v_pk_mul_f32 v[214:215], v[216:217], v[214:215]
	v_pk_mul_f32 v[212:213], v[218:219], v[212:213]
	v_exp_f32_e32 v205, v205
	v_exp_f32_e32 v206, v206
	v_exp_f32_e32 v207, v207
	v_exp_f32_e32 v212, v212
	v_exp_f32_e32 v214, v214
	v_exp_f32_e32 v215, v215
	v_exp_f32_e32 v213, v213
	v_pk_add_f32 v[206:207], v[206:207], 1.0 op_sel_hi:[1,0]
	v_pk_add_f32 v[204:205], v[204:205], 1.0 op_sel_hi:[1,0]
	v_pk_add_f32 v[214:215], v[214:215], 1.0 op_sel_hi:[1,0]
	v_pk_add_f32 v[212:213], v[212:213], 1.0 op_sel_hi:[1,0]
	v_rcp_f32_e32 v204, v204
	v_rcp_f32_e32 v205, v205
	v_rcp_f32_e32 v206, v206
	v_rcp_f32_e32 v207, v207
	v_rcp_f32_e32 v211, v212
	v_rcp_f32_e32 v212, v213
	v_rcp_f32_e32 v213, v214
	v_rcp_f32_e32 v214, v215
	v_cvt_pk_bf16_f32 v204, v204, v205
	v_cvt_pk_bf16_f32 v205, v206, v207
	v_cvt_pk_bf16_f32 v206, v211, v212
	v_cvt_pk_bf16_f32 v207, v213, v214
	global_store_dwordx4 v[208:209], v[204:207], off nt
	v_pk_mul_f32 v[212:213], v[108:109], v[210:211] op_sel_hi:[1,0]
	v_pk_mul_f32 v[214:215], v[106:107], v[210:211] op_sel_hi:[1,0]
	v_cvt_f32_i32_e32 v205, v59
	v_cvt_f32_i32_e32 v207, v61
	v_cvt_f32_i32_e32 v206, v60
	v_cvt_f32_i32_e32 v204, v58
	v_pk_mul_f32 v[216:217], v[112:113], v[210:211] op_sel_hi:[1,0]
	v_pk_mul_f32 v[210:211], v[110:111], v[210:211] op_sel_hi:[1,0]
	v_pk_mul_f32 v[206:207], v[212:213], v[206:207]
	v_pk_mul_f32 v[204:205], v[214:215], v[204:205]
	v_cvt_f32_i32_e32 v213, v71
	v_cvt_f32_i32_e32 v215, v73
	v_cvt_f32_i32_e32 v214, v72
	v_cvt_f32_i32_e32 v212, v70
	v_exp_f32_e32 v204, v204
	v_exp_f32_e32 v205, v205
	v_pk_mul_f32 v[214:215], v[216:217], v[214:215]
	v_pk_mul_f32 v[210:211], v[210:211], v[212:213]
	v_exp_f32_e32 v206, v206
	v_exp_f32_e32 v207, v207
	v_exp_f32_e32 v210, v210
	v_exp_f32_e32 v212, v214
	v_exp_f32_e32 v213, v215
	v_exp_f32_e32 v211, v211
	v_pk_add_f32 v[204:205], v[204:205], 1.0 op_sel_hi:[1,0]
	v_pk_add_f32 v[206:207], v[206:207], 1.0 op_sel_hi:[1,0]
	v_rcp_f32_e32 v204, v204
	v_pk_add_f32 v[212:213], v[212:213], 1.0 op_sel_hi:[1,0]
	v_pk_add_f32 v[210:211], v[210:211], 1.0 op_sel_hi:[1,0]
	v_rcp_f32_e32 v205, v205
	v_rcp_f32_e32 v206, v206
	v_rcp_f32_e32 v207, v207
	v_cvt_pk_bf16_f32 v204, v204, v205
	v_rcp_f32_e32 v210, v210
	v_rcp_f32_e32 v211, v211
	v_rcp_f32_e32 v212, v212
	v_rcp_f32_e32 v213, v213
	v_cvt_pk_bf16_f32 v205, v206, v207
	v_cvt_pk_bf16_f32 v206, v210, v211
	v_cvt_pk_bf16_f32 v207, v212, v213
	global_store_dwordx4 v[208:209], v[204:207], off offset:256 nt
	v_mul_f32_e32 v210, 0xbfb8aa3b, v184
	v_pk_mul_f32 v[212:213], v[116:117], v[210:211] op_sel_hi:[1,0]
	v_add_u32_e32 v204, 0x80, v146
	v_mad_i64_i32 v[204:205], s[0:1], v204, s58, v[192:193]
	v_lshl_add_u64 v[208:209], v[204:205], 0, v[194:195]
	v_cvt_f32_i32_e32 v205, v55
	v_cvt_f32_i32_e32 v207, v57
	v_cvt_f32_i32_e32 v206, v56
	v_cvt_f32_i32_e32 v204, v54
	v_pk_mul_f32 v[214:215], v[114:115], v[210:211] op_sel_hi:[1,0]
	v_pk_mul_f32 v[216:217], v[120:121], v[210:211] op_sel_hi:[1,0]
	v_pk_mul_f32 v[206:207], v[212:213], v[206:207]
	v_pk_mul_f32 v[204:205], v[214:215], v[204:205]
	v_cvt_f32_i32_e32 v213, v51
	v_cvt_f32_i32_e32 v215, v53
	v_cvt_f32_i32_e32 v214, v52
	v_cvt_f32_i32_e32 v212, v50
	v_pk_mul_f32 v[218:219], v[118:119], v[210:211] op_sel_hi:[1,0]
	v_exp_f32_e32 v204, v204
	v_pk_mul_f32 v[214:215], v[216:217], v[214:215]
	v_pk_mul_f32 v[212:213], v[218:219], v[212:213]
	v_exp_f32_e32 v205, v205
	v_exp_f32_e32 v206, v206
	v_exp_f32_e32 v207, v207
	v_exp_f32_e32 v212, v212
	v_exp_f32_e32 v214, v214
	v_exp_f32_e32 v215, v215
	v_exp_f32_e32 v213, v213
	v_pk_add_f32 v[206:207], v[206:207], 1.0 op_sel_hi:[1,0]
	v_pk_add_f32 v[204:205], v[204:205], 1.0 op_sel_hi:[1,0]
	v_pk_add_f32 v[214:215], v[214:215], 1.0 op_sel_hi:[1,0]
	v_pk_add_f32 v[212:213], v[212:213], 1.0 op_sel_hi:[1,0]
	v_rcp_f32_e32 v204, v204
	v_rcp_f32_e32 v205, v205
	v_rcp_f32_e32 v206, v206
	v_rcp_f32_e32 v207, v207
	v_rcp_f32_e32 v211, v212
	v_rcp_f32_e32 v212, v213
	v_rcp_f32_e32 v213, v214
	v_rcp_f32_e32 v214, v215
	v_cvt_pk_bf16_f32 v204, v204, v205
	v_cvt_pk_bf16_f32 v205, v206, v207
	v_cvt_pk_bf16_f32 v206, v211, v212
	v_cvt_pk_bf16_f32 v207, v213, v214
	global_store_dwordx4 v[208:209], v[204:207], off nt
	v_pk_mul_f32 v[212:213], v[108:109], v[210:211] op_sel_hi:[1,0]
	v_pk_mul_f32 v[214:215], v[106:107], v[210:211] op_sel_hi:[1,0]
	v_cvt_f32_i32_e32 v205, v67
	v_cvt_f32_i32_e32 v207, v69
	v_cvt_f32_i32_e32 v206, v68
	v_cvt_f32_i32_e32 v204, v66
	v_pk_mul_f32 v[216:217], v[112:113], v[210:211] op_sel_hi:[1,0]
	v_pk_mul_f32 v[210:211], v[110:111], v[210:211] op_sel_hi:[1,0]
	v_pk_mul_f32 v[206:207], v[212:213], v[206:207]
	v_pk_mul_f32 v[204:205], v[214:215], v[204:205]
	v_cvt_f32_i32_e32 v213, v63
	v_cvt_f32_i32_e32 v215, v65
	v_cvt_f32_i32_e32 v214, v64
	v_cvt_f32_i32_e32 v212, v62
	v_exp_f32_e32 v204, v204
	v_exp_f32_e32 v205, v205
	v_pk_mul_f32 v[214:215], v[216:217], v[214:215]
	v_pk_mul_f32 v[210:211], v[210:211], v[212:213]
	v_exp_f32_e32 v206, v206
	v_exp_f32_e32 v207, v207
	v_exp_f32_e32 v210, v210
	v_exp_f32_e32 v212, v214
	v_exp_f32_e32 v213, v215
	v_exp_f32_e32 v211, v211
	v_pk_add_f32 v[204:205], v[204:205], 1.0 op_sel_hi:[1,0]
	v_pk_add_f32 v[206:207], v[206:207], 1.0 op_sel_hi:[1,0]
	v_rcp_f32_e32 v204, v204
	v_pk_add_f32 v[212:213], v[212:213], 1.0 op_sel_hi:[1,0]
	v_pk_add_f32 v[210:211], v[210:211], 1.0 op_sel_hi:[1,0]
	v_rcp_f32_e32 v205, v205
	v_rcp_f32_e32 v206, v206
	v_rcp_f32_e32 v207, v207
	v_cvt_pk_bf16_f32 v204, v204, v205
	v_rcp_f32_e32 v210, v210
	v_rcp_f32_e32 v211, v211
	v_rcp_f32_e32 v212, v212
	v_rcp_f32_e32 v213, v213
	v_cvt_pk_bf16_f32 v205, v206, v207
	v_cvt_pk_bf16_f32 v206, v210, v211
	v_cvt_pk_bf16_f32 v207, v212, v213
	global_store_dwordx4 v[208:209], v[204:207], off offset:256 nt
	v_mul_f32_e32 v210, 0xbfb8aa3b, v185
	v_pk_mul_f32 v[212:213], v[116:117], v[210:211] op_sel_hi:[1,0]
	v_add_u32_e32 v204, 0x90, v146
	v_mad_i64_i32 v[204:205], s[0:1], v204, s58, v[192:193]
	v_lshl_add_u64 v[208:209], v[204:205], 0, v[194:195]
	v_cvt_f32_i32_e32 v205, v35
	v_cvt_f32_i32_e32 v207, v37
	v_cvt_f32_i32_e32 v206, v36
	v_cvt_f32_i32_e32 v204, v34
	v_pk_mul_f32 v[214:215], v[114:115], v[210:211] op_sel_hi:[1,0]
	v_pk_mul_f32 v[216:217], v[120:121], v[210:211] op_sel_hi:[1,0]
	v_pk_mul_f32 v[206:207], v[212:213], v[206:207]
	v_pk_mul_f32 v[204:205], v[214:215], v[204:205]
	v_cvt_f32_i32_e32 v213, v39
	v_cvt_f32_i32_e32 v215, v41
	v_cvt_f32_i32_e32 v214, v40
	v_cvt_f32_i32_e32 v212, v38
	v_pk_mul_f32 v[218:219], v[118:119], v[210:211] op_sel_hi:[1,0]
	v_exp_f32_e32 v204, v204
	v_pk_mul_f32 v[214:215], v[216:217], v[214:215]
	v_pk_mul_f32 v[212:213], v[218:219], v[212:213]
	v_exp_f32_e32 v205, v205
	v_exp_f32_e32 v206, v206
	v_exp_f32_e32 v207, v207
	v_exp_f32_e32 v212, v212
	v_exp_f32_e32 v214, v214
	v_exp_f32_e32 v215, v215
	v_exp_f32_e32 v213, v213
	v_pk_add_f32 v[206:207], v[206:207], 1.0 op_sel_hi:[1,0]
	v_pk_add_f32 v[204:205], v[204:205], 1.0 op_sel_hi:[1,0]
	v_pk_add_f32 v[214:215], v[214:215], 1.0 op_sel_hi:[1,0]
	v_pk_add_f32 v[212:213], v[212:213], 1.0 op_sel_hi:[1,0]
	v_rcp_f32_e32 v204, v204
	v_rcp_f32_e32 v205, v205
	v_rcp_f32_e32 v206, v206
	v_rcp_f32_e32 v207, v207
	v_rcp_f32_e32 v211, v212
	v_rcp_f32_e32 v212, v213
	v_rcp_f32_e32 v213, v214
	v_rcp_f32_e32 v214, v215
	v_cvt_pk_bf16_f32 v204, v204, v205
	v_cvt_pk_bf16_f32 v205, v206, v207
	v_cvt_pk_bf16_f32 v206, v211, v212
	v_cvt_pk_bf16_f32 v207, v213, v214
	global_store_dwordx4 v[208:209], v[204:207], off nt
	v_pk_mul_f32 v[212:213], v[108:109], v[210:211] op_sel_hi:[1,0]
	v_pk_mul_f32 v[214:215], v[106:107], v[210:211] op_sel_hi:[1,0]
	v_cvt_f32_i32_e32 v205, v43
	v_cvt_f32_i32_e32 v207, v45
	v_cvt_f32_i32_e32 v206, v44
	v_cvt_f32_i32_e32 v204, v42
	v_pk_mul_f32 v[216:217], v[112:113], v[210:211] op_sel_hi:[1,0]
	v_pk_mul_f32 v[210:211], v[110:111], v[210:211] op_sel_hi:[1,0]
	v_pk_mul_f32 v[206:207], v[212:213], v[206:207]
	v_pk_mul_f32 v[204:205], v[214:215], v[204:205]
	v_cvt_f32_i32_e32 v213, v47
	v_cvt_f32_i32_e32 v215, v49
	v_cvt_f32_i32_e32 v214, v48
	v_cvt_f32_i32_e32 v212, v46
	v_exp_f32_e32 v204, v204
	v_exp_f32_e32 v205, v205
	v_pk_mul_f32 v[214:215], v[216:217], v[214:215]
	v_pk_mul_f32 v[210:211], v[210:211], v[212:213]
	v_exp_f32_e32 v206, v206
	v_exp_f32_e32 v207, v207
	v_exp_f32_e32 v210, v210
	v_exp_f32_e32 v212, v214
	v_exp_f32_e32 v213, v215
	v_exp_f32_e32 v211, v211
	v_pk_add_f32 v[204:205], v[204:205], 1.0 op_sel_hi:[1,0]
	v_pk_add_f32 v[206:207], v[206:207], 1.0 op_sel_hi:[1,0]
	v_rcp_f32_e32 v204, v204
	v_pk_add_f32 v[212:213], v[212:213], 1.0 op_sel_hi:[1,0]
	v_pk_add_f32 v[210:211], v[210:211], 1.0 op_sel_hi:[1,0]
	v_rcp_f32_e32 v205, v205
	v_rcp_f32_e32 v206, v206
	v_rcp_f32_e32 v207, v207
	v_cvt_pk_bf16_f32 v204, v204, v205
	v_rcp_f32_e32 v210, v210
	v_rcp_f32_e32 v211, v211
	v_rcp_f32_e32 v212, v212
	v_rcp_f32_e32 v213, v213
	v_cvt_pk_bf16_f32 v205, v206, v207
	v_cvt_pk_bf16_f32 v206, v210, v211
	v_cvt_pk_bf16_f32 v207, v212, v213
	global_store_dwordx4 v[208:209], v[204:207], off offset:256 nt
	v_mul_f32_e32 v210, 0xbfb8aa3b, v182
	v_pk_mul_f32 v[212:213], v[116:117], v[210:211] op_sel_hi:[1,0]
	v_add_u32_e32 v204, 0xa0, v146
	v_mad_i64_i32 v[204:205], s[0:1], v204, s58, v[192:193]
	v_lshl_add_u64 v[208:209], v[204:205], 0, v[194:195]
	v_cvt_f32_i32_e32 v205, v23
	v_cvt_f32_i32_e32 v207, v25
	v_cvt_f32_i32_e32 v206, v24
	v_cvt_f32_i32_e32 v204, v22
	v_pk_mul_f32 v[214:215], v[114:115], v[210:211] op_sel_hi:[1,0]
	v_pk_mul_f32 v[216:217], v[120:121], v[210:211] op_sel_hi:[1,0]
	v_pk_mul_f32 v[206:207], v[212:213], v[206:207]
	v_pk_mul_f32 v[204:205], v[214:215], v[204:205]
	v_cvt_f32_i32_e32 v213, v19
	v_cvt_f32_i32_e32 v215, v21
	v_cvt_f32_i32_e32 v214, v20
	v_cvt_f32_i32_e32 v212, v18
	v_pk_mul_f32 v[218:219], v[118:119], v[210:211] op_sel_hi:[1,0]
	v_exp_f32_e32 v204, v204
	v_pk_mul_f32 v[214:215], v[216:217], v[214:215]
	v_pk_mul_f32 v[212:213], v[218:219], v[212:213]
	v_exp_f32_e32 v205, v205
	v_exp_f32_e32 v206, v206
	v_exp_f32_e32 v207, v207
	v_exp_f32_e32 v212, v212
	v_exp_f32_e32 v214, v214
	v_exp_f32_e32 v215, v215
	v_exp_f32_e32 v213, v213
	v_pk_add_f32 v[206:207], v[206:207], 1.0 op_sel_hi:[1,0]
	v_pk_add_f32 v[204:205], v[204:205], 1.0 op_sel_hi:[1,0]
	v_pk_add_f32 v[214:215], v[214:215], 1.0 op_sel_hi:[1,0]
	v_pk_add_f32 v[212:213], v[212:213], 1.0 op_sel_hi:[1,0]
	v_rcp_f32_e32 v204, v204
	v_rcp_f32_e32 v205, v205
	v_rcp_f32_e32 v206, v206
	v_rcp_f32_e32 v207, v207
	v_rcp_f32_e32 v211, v212
	v_rcp_f32_e32 v212, v213
	v_rcp_f32_e32 v213, v214
	v_rcp_f32_e32 v214, v215
	v_cvt_pk_bf16_f32 v204, v204, v205
	v_cvt_pk_bf16_f32 v205, v206, v207
	v_cvt_pk_bf16_f32 v206, v211, v212
	v_cvt_pk_bf16_f32 v207, v213, v214
	global_store_dwordx4 v[208:209], v[204:207], off nt
	v_pk_mul_f32 v[212:213], v[108:109], v[210:211] op_sel_hi:[1,0]
	v_pk_mul_f32 v[214:215], v[106:107], v[210:211] op_sel_hi:[1,0]
	v_cvt_f32_i32_e32 v205, v31
	v_cvt_f32_i32_e32 v207, v33
	v_cvt_f32_i32_e32 v206, v32
	v_cvt_f32_i32_e32 v204, v30
	v_pk_mul_f32 v[216:217], v[112:113], v[210:211] op_sel_hi:[1,0]
	v_pk_mul_f32 v[210:211], v[110:111], v[210:211] op_sel_hi:[1,0]
	v_pk_mul_f32 v[206:207], v[212:213], v[206:207]
	v_pk_mul_f32 v[204:205], v[214:215], v[204:205]
	v_cvt_f32_i32_e32 v213, v27
	v_cvt_f32_i32_e32 v215, v29
	v_cvt_f32_i32_e32 v214, v28
	v_cvt_f32_i32_e32 v212, v26
	v_exp_f32_e32 v204, v204
	v_exp_f32_e32 v205, v205
	v_pk_mul_f32 v[214:215], v[216:217], v[214:215]
	v_pk_mul_f32 v[210:211], v[210:211], v[212:213]
	v_exp_f32_e32 v206, v206
	v_exp_f32_e32 v207, v207
	v_exp_f32_e32 v210, v210
	v_exp_f32_e32 v212, v214
	v_exp_f32_e32 v213, v215
	v_exp_f32_e32 v211, v211
	v_pk_add_f32 v[204:205], v[204:205], 1.0 op_sel_hi:[1,0]
	v_pk_add_f32 v[206:207], v[206:207], 1.0 op_sel_hi:[1,0]
	v_rcp_f32_e32 v204, v204
	v_pk_add_f32 v[212:213], v[212:213], 1.0 op_sel_hi:[1,0]
	v_pk_add_f32 v[210:211], v[210:211], 1.0 op_sel_hi:[1,0]
	v_rcp_f32_e32 v205, v205
	v_rcp_f32_e32 v206, v206
	v_rcp_f32_e32 v207, v207
	v_cvt_pk_bf16_f32 v204, v204, v205
	v_rcp_f32_e32 v210, v210
	v_rcp_f32_e32 v211, v211
	v_rcp_f32_e32 v212, v212
	v_rcp_f32_e32 v213, v213
	v_cvt_pk_bf16_f32 v205, v206, v207
	v_cvt_pk_bf16_f32 v206, v210, v211
	v_cvt_pk_bf16_f32 v207, v212, v213
	global_store_dwordx4 v[208:209], v[204:207], off offset:256 nt
	s_nop 1
	v_add_u32_e32 v204, 0xb0, v146
	v_mad_i64_i32 v[192:193], s[0:1], v204, s58, v[192:193]
	v_lshl_add_u64 v[204:205], v[192:193], 0, v[194:195]
	v_cvt_f32_i32_e32 v193, v3
	v_cvt_f32_i32_e32 v195, v5
	v_cvt_f32_i32_e32 v194, v4
	v_cvt_f32_i32_e32 v192, v2
	v_mul_f32_e32 v206, 0xbfb8aa3b, v183
	v_pk_mul_f32 v[208:209], v[116:117], v[206:207] op_sel_hi:[1,0]
	v_pk_mul_f32 v[210:211], v[114:115], v[206:207] op_sel_hi:[1,0]
	v_pk_mul_f32 v[194:195], v[208:209], v[194:195]
	v_pk_mul_f32 v[192:193], v[210:211], v[192:193]
	v_cvt_f32_i32_e32 v209, v7
	v_cvt_f32_i32_e32 v211, v9
	v_cvt_f32_i32_e32 v210, v8
	v_cvt_f32_i32_e32 v208, v6
	v_pk_mul_f32 v[212:213], v[120:121], v[206:207] op_sel_hi:[1,0]
	v_pk_mul_f32 v[214:215], v[118:119], v[206:207] op_sel_hi:[1,0]
	v_pk_mul_f32 v[210:211], v[212:213], v[210:211]
	v_pk_mul_f32 v[208:209], v[214:215], v[208:209]
	v_exp_f32_e32 v192, v192
	v_exp_f32_e32 v193, v193
	v_exp_f32_e32 v194, v194
	v_exp_f32_e32 v195, v195
	v_exp_f32_e32 v208, v208
	v_exp_f32_e32 v210, v210
	v_exp_f32_e32 v211, v211
	v_exp_f32_e32 v209, v209
	v_pk_add_f32 v[194:195], v[194:195], 1.0 op_sel_hi:[1,0]
	v_pk_add_f32 v[192:193], v[192:193], 1.0 op_sel_hi:[1,0]
	v_pk_add_f32 v[210:211], v[210:211], 1.0 op_sel_hi:[1,0]
	v_pk_add_f32 v[208:209], v[208:209], 1.0 op_sel_hi:[1,0]
	v_rcp_f32_e32 v192, v192
	v_rcp_f32_e32 v193, v193
	v_rcp_f32_e32 v194, v194
	v_rcp_f32_e32 v195, v195
	v_rcp_f32_e32 v207, v208
	v_rcp_f32_e32 v208, v209
	v_rcp_f32_e32 v209, v210
	v_rcp_f32_e32 v210, v211
	v_cvt_pk_bf16_f32 v192, v192, v193
	v_cvt_pk_bf16_f32 v193, v194, v195
	v_cvt_pk_bf16_f32 v194, v207, v208
	v_cvt_pk_bf16_f32 v195, v209, v210
	global_store_dwordx4 v[204:205], v[192:195], off nt
	v_pk_mul_f32 v[208:209], v[108:109], v[206:207] op_sel_hi:[1,0]
	v_pk_mul_f32 v[210:211], v[106:107], v[206:207] op_sel_hi:[1,0]
	v_cvt_f32_i32_e32 v193, v11
	v_cvt_f32_i32_e32 v195, v13
	v_cvt_f32_i32_e32 v194, v12
	v_cvt_f32_i32_e32 v192, v10
	v_pk_mul_f32 v[212:213], v[112:113], v[206:207] op_sel_hi:[1,0]
	v_pk_mul_f32 v[206:207], v[110:111], v[206:207] op_sel_hi:[1,0]
	v_pk_mul_f32 v[194:195], v[208:209], v[194:195]
	v_pk_mul_f32 v[192:193], v[210:211], v[192:193]
	v_cvt_f32_i32_e32 v209, v15
	v_cvt_f32_i32_e32 v211, v17
	v_cvt_f32_i32_e32 v210, v16
	v_cvt_f32_i32_e32 v208, v14
	v_exp_f32_e32 v192, v192
	v_exp_f32_e32 v193, v193
	v_pk_mul_f32 v[210:211], v[212:213], v[210:211]
	v_pk_mul_f32 v[206:207], v[206:207], v[208:209]
	v_exp_f32_e32 v194, v194
	v_exp_f32_e32 v195, v195
	v_exp_f32_e32 v206, v206
	v_exp_f32_e32 v208, v210
	v_exp_f32_e32 v209, v211
	v_exp_f32_e32 v207, v207
	v_pk_add_f32 v[194:195], v[194:195], 1.0 op_sel_hi:[1,0]
	v_pk_add_f32 v[192:193], v[192:193], 1.0 op_sel_hi:[1,0]
	v_pk_add_f32 v[208:209], v[208:209], 1.0 op_sel_hi:[1,0]
	v_pk_add_f32 v[206:207], v[206:207], 1.0 op_sel_hi:[1,0]
	v_rcp_f32_e32 v192, v192
	v_rcp_f32_e32 v193, v193
	v_rcp_f32_e32 v194, v194
	v_rcp_f32_e32 v195, v195
	v_rcp_f32_e32 v206, v206
	v_rcp_f32_e32 v207, v207
	v_rcp_f32_e32 v208, v208
	v_rcp_f32_e32 v209, v209
	v_cvt_pk_bf16_f32 v192, v192, v193
	v_cvt_pk_bf16_f32 v193, v194, v195
	v_cvt_pk_bf16_f32 v194, v206, v207
	v_cvt_pk_bf16_f32 v195, v208, v209
	global_store_dwordx4 v[204:205], v[192:195], off offset:256 nt
	s_mov_b64 s[0:1], 0
